# stack: DPP-scan threshold search (both DSA copies) + unrolled pass-1 tile body also in the half-block copy + batched build_q loads
# baseline (speedup 1.0000x reference)
.LBB0_510:
	v_readlane_b32 s0, v252, 20
	s_waitcnt lgkmcnt(1)
	v_add_u32_e32 v7, 0, v52
	s_cmp_gt_i32 s49, s0
	v_lshlrev_b32_e32 v6, 2, v42
	s_waitcnt lgkmcnt(0)
	s_barrier
	s_waitcnt vmcnt(2)
	s_cbranch_scc0 .Lthr_none_a
	s_lshl_b32 s12, s96, 13
	v_add_u32_e32 v72, s12, v7
	ds_read_b128 v[76:79], v72 offset:32768
	ds_read_b128 v[80:83], v72 offset:33792
	ds_read_b128 v[84:87], v72 offset:34816
	ds_read_b128 v[88:91], v72 offset:35840
	ds_read_b128 v[92:95], v72 offset:36864
	ds_read_b128 v[96:99], v72 offset:37888
	ds_read_b128 v[100:103], v72 offset:38912
	ds_read_b128 v[104:107], v72 offset:39936
	s_lshl_b32 s31, s96, 7
	s_add_i32 s31, s31, 0x23000
	v_mov_b32_e32 v118, s31
	v_mov_b32_e32 v117, 0
	s_waitcnt lgkmcnt(0)
	v_add_u32_e32 v73, v76, v77
	v_add3_u32 v74, v73, v78, v79
	s_nop 1
	v_add_u32_dpp v74, v74, v74 row_shr:1 row_mask:0xf bank_mask:0xf
	s_nop 1
	v_add_u32_dpp v74, v74, v74 row_shr:2 row_mask:0xf bank_mask:0xf
	s_nop 1
	v_add_u32_dpp v74, v74, v74 row_shr:4 row_mask:0xf bank_mask:0xf
	s_nop 1
	v_add_u32_dpp v74, v74, v74 row_shr:8 row_mask:0xf bank_mask:0xf
	s_nop 1
	v_add_u32_dpp v74, v74, v74 row_bcast:15 row_mask:0xa bank_mask:0xf
	s_nop 1
	v_add_u32_dpp v74, v74, v74 row_bcast:31 row_mask:0xc bank_mask:0xf
	v_mov_b32_e32 v108, -1
	v_mov_b32_e32 v109, 0
	v_readlane_b32 s13, v74, 63
	v_mov_b32_e32 v110, 0
	s_nop 0
	v_sub_u32_e32 v75, s13, v74
	v_add_u32_e32 v111, v75, v79
	v_cmp_gt_i32_e32 vcc, 0x100, v75
	v_cmp_le_i32_e64 s[0:1], s87, v111
	v_or_b32_e32 v112, 3, v6
	s_and_b64 vcc, vcc, s[0:1]
	v_cndmask_b32_e32 v108, v108, v112, vcc
	v_cndmask_b32_e32 v109, v109, v75, vcc
	v_cndmask_b32_e32 v110, v110, v79, vcc
	v_mov_b32_e32 v75, v111
	v_add_u32_e32 v111, v75, v78
	v_cmp_gt_i32_e32 vcc, 0x100, v75
	v_cmp_le_i32_e64 s[0:1], s87, v111
	v_or_b32_e32 v112, 2, v6
	s_and_b64 vcc, vcc, s[0:1]
	v_cndmask_b32_e32 v108, v108, v112, vcc
	v_cndmask_b32_e32 v109, v109, v75, vcc
	v_cndmask_b32_e32 v110, v110, v78, vcc
	v_mov_b32_e32 v75, v111
	v_add_u32_e32 v111, v75, v77
	v_cmp_gt_i32_e32 vcc, 0x100, v75
	v_cmp_le_i32_e64 s[0:1], s87, v111
	v_or_b32_e32 v112, 1, v6
	s_and_b64 vcc, vcc, s[0:1]
	v_cndmask_b32_e32 v108, v108, v112, vcc
	v_cndmask_b32_e32 v109, v109, v75, vcc
	v_cndmask_b32_e32 v110, v110, v77, vcc
	v_mov_b32_e32 v75, v111
	v_add_u32_e32 v111, v75, v76
	v_cmp_gt_i32_e32 vcc, 0x100, v75
	v_cmp_le_i32_e64 s[0:1], s87, v111
	v_or_b32_e32 v112, 0, v6
	s_and_b64 vcc, vcc, s[0:1]
	v_cndmask_b32_e32 v108, v108, v112, vcc
	v_cndmask_b32_e32 v109, v109, v75, vcc
	v_cndmask_b32_e32 v110, v110, v76, vcc
	v_mov_b32_e32 v75, v111
	v_cmp_lt_i32_e32 vcc, -1, v108
	s_ff1_i32_b64 s0, vcc
	s_cmp_lg_u64 vcc, 0
	s_cselect_b32 s0, s0, 0
	v_readlane_b32 s1, v109, s0
	v_readlane_b32 s12, v108, s0
	v_readlane_b32 s13, v110, s0
	s_sub_i32 s30, 0x100, s1
	s_nop 0
	v_mov_b32_e32 v114, s12
	v_mov_b32_e32 v115, s30
	v_mov_b32_e32 v116, s13
	s_and_saveexec_b64 s[0:1], s[26:27]
	ds_write_b128 v118, v[114:117]
	s_or_b64 exec, exec, s[0:1]
	v_add_u32_e32 v73, v80, v81
	v_add3_u32 v74, v73, v82, v83
	s_nop 1
	v_add_u32_dpp v74, v74, v74 row_shr:1 row_mask:0xf bank_mask:0xf
	s_nop 1
	v_add_u32_dpp v74, v74, v74 row_shr:2 row_mask:0xf bank_mask:0xf
	s_nop 1
	v_add_u32_dpp v74, v74, v74 row_shr:4 row_mask:0xf bank_mask:0xf
	s_nop 1
	v_add_u32_dpp v74, v74, v74 row_shr:8 row_mask:0xf bank_mask:0xf
	s_nop 1
	v_add_u32_dpp v74, v74, v74 row_bcast:15 row_mask:0xa bank_mask:0xf
	s_nop 1
	v_add_u32_dpp v74, v74, v74 row_bcast:31 row_mask:0xc bank_mask:0xf
	v_mov_b32_e32 v108, -1
	v_mov_b32_e32 v109, 0
	v_readlane_b32 s13, v74, 63
	v_mov_b32_e32 v110, 0
	s_nop 0
	v_sub_u32_e32 v75, s13, v74
	v_add_u32_e32 v111, v75, v83
	v_cmp_gt_i32_e32 vcc, 0x100, v75
	v_cmp_le_i32_e64 s[0:1], s87, v111
	v_or_b32_e32 v112, 3, v6
	s_and_b64 vcc, vcc, s[0:1]
	v_cndmask_b32_e32 v108, v108, v112, vcc
	v_cndmask_b32_e32 v109, v109, v75, vcc
	v_cndmask_b32_e32 v110, v110, v83, vcc
	v_mov_b32_e32 v75, v111
	v_add_u32_e32 v111, v75, v82
	v_cmp_gt_i32_e32 vcc, 0x100, v75
	v_cmp_le_i32_e64 s[0:1], s87, v111
	v_or_b32_e32 v112, 2, v6
	s_and_b64 vcc, vcc, s[0:1]
	v_cndmask_b32_e32 v108, v108, v112, vcc
	v_cndmask_b32_e32 v109, v109, v75, vcc
	v_cndmask_b32_e32 v110, v110, v82, vcc
	v_mov_b32_e32 v75, v111
	v_add_u32_e32 v111, v75, v81
	v_cmp_gt_i32_e32 vcc, 0x100, v75
	v_cmp_le_i32_e64 s[0:1], s87, v111
	v_or_b32_e32 v112, 1, v6
	s_and_b64 vcc, vcc, s[0:1]
	v_cndmask_b32_e32 v108, v108, v112, vcc
	v_cndmask_b32_e32 v109, v109, v75, vcc
	v_cndmask_b32_e32 v110, v110, v81, vcc
	v_mov_b32_e32 v75, v111
	v_add_u32_e32 v111, v75, v80
	v_cmp_gt_i32_e32 vcc, 0x100, v75
	v_cmp_le_i32_e64 s[0:1], s87, v111
	v_or_b32_e32 v112, 0, v6
	s_and_b64 vcc, vcc, s[0:1]
	v_cndmask_b32_e32 v108, v108, v112, vcc
	v_cndmask_b32_e32 v109, v109, v75, vcc
	v_cndmask_b32_e32 v110, v110, v80, vcc
	v_mov_b32_e32 v75, v111
	v_cmp_lt_i32_e32 vcc, -1, v108
	s_ff1_i32_b64 s0, vcc
	s_cmp_lg_u64 vcc, 0
	s_cselect_b32 s0, s0, 0
	v_readlane_b32 s1, v109, s0
	v_readlane_b32 s12, v108, s0
	v_readlane_b32 s13, v110, s0
	s_sub_i32 s30, 0x100, s1
	s_nop 0
	v_mov_b32_e32 v114, s12
	v_mov_b32_e32 v115, s30
	v_mov_b32_e32 v116, s13
	s_and_saveexec_b64 s[0:1], s[26:27]
	ds_write_b128 v118, v[114:117] offset:16
	s_or_b64 exec, exec, s[0:1]
	v_add_u32_e32 v73, v84, v85
	v_add3_u32 v74, v73, v86, v87
	s_nop 1
	v_add_u32_dpp v74, v74, v74 row_shr:1 row_mask:0xf bank_mask:0xf
	s_nop 1
	v_add_u32_dpp v74, v74, v74 row_shr:2 row_mask:0xf bank_mask:0xf
	s_nop 1
	v_add_u32_dpp v74, v74, v74 row_shr:4 row_mask:0xf bank_mask:0xf
	s_nop 1
	v_add_u32_dpp v74, v74, v74 row_shr:8 row_mask:0xf bank_mask:0xf
	s_nop 1
	v_add_u32_dpp v74, v74, v74 row_bcast:15 row_mask:0xa bank_mask:0xf
	s_nop 1
	v_add_u32_dpp v74, v74, v74 row_bcast:31 row_mask:0xc bank_mask:0xf
	v_mov_b32_e32 v108, -1
	v_mov_b32_e32 v109, 0
	v_readlane_b32 s13, v74, 63
	v_mov_b32_e32 v110, 0
	s_nop 0
	v_sub_u32_e32 v75, s13, v74
	v_add_u32_e32 v111, v75, v87
	v_cmp_gt_i32_e32 vcc, 0x100, v75
	v_cmp_le_i32_e64 s[0:1], s87, v111
	v_or_b32_e32 v112, 3, v6
	s_and_b64 vcc, vcc, s[0:1]
	v_cndmask_b32_e32 v108, v108, v112, vcc
	v_cndmask_b32_e32 v109, v109, v75, vcc
	v_cndmask_b32_e32 v110, v110, v87, vcc
	v_mov_b32_e32 v75, v111
	v_add_u32_e32 v111, v75, v86
	v_cmp_gt_i32_e32 vcc, 0x100, v75
	v_cmp_le_i32_e64 s[0:1], s87, v111
	v_or_b32_e32 v112, 2, v6
	s_and_b64 vcc, vcc, s[0:1]
	v_cndmask_b32_e32 v108, v108, v112, vcc
	v_cndmask_b32_e32 v109, v109, v75, vcc
	v_cndmask_b32_e32 v110, v110, v86, vcc
	v_mov_b32_e32 v75, v111
	v_add_u32_e32 v111, v75, v85
	v_cmp_gt_i32_e32 vcc, 0x100, v75
	v_cmp_le_i32_e64 s[0:1], s87, v111
	v_or_b32_e32 v112, 1, v6
	s_and_b64 vcc, vcc, s[0:1]
	v_cndmask_b32_e32 v108, v108, v112, vcc
	v_cndmask_b32_e32 v109, v109, v75, vcc
	v_cndmask_b32_e32 v110, v110, v85, vcc
	v_mov_b32_e32 v75, v111
	v_add_u32_e32 v111, v75, v84
	v_cmp_gt_i32_e32 vcc, 0x100, v75
	v_cmp_le_i32_e64 s[0:1], s87, v111
	v_or_b32_e32 v112, 0, v6
	s_and_b64 vcc, vcc, s[0:1]
	v_cndmask_b32_e32 v108, v108, v112, vcc
	v_cndmask_b32_e32 v109, v109, v75, vcc
	v_cndmask_b32_e32 v110, v110, v84, vcc
	v_mov_b32_e32 v75, v111
	v_cmp_lt_i32_e32 vcc, -1, v108
	s_ff1_i32_b64 s0, vcc
	s_cmp_lg_u64 vcc, 0
	s_cselect_b32 s0, s0, 0
	v_readlane_b32 s1, v109, s0
	v_readlane_b32 s12, v108, s0
	v_readlane_b32 s13, v110, s0
	s_sub_i32 s30, 0x100, s1
	s_nop 0
	v_mov_b32_e32 v114, s12
	v_mov_b32_e32 v115, s30
	v_mov_b32_e32 v116, s13
	s_and_saveexec_b64 s[0:1], s[26:27]
	ds_write_b128 v118, v[114:117] offset:32
	s_or_b64 exec, exec, s[0:1]
	v_add_u32_e32 v73, v88, v89
	v_add3_u32 v74, v73, v90, v91
	s_nop 1
	v_add_u32_dpp v74, v74, v74 row_shr:1 row_mask:0xf bank_mask:0xf
	s_nop 1
	v_add_u32_dpp v74, v74, v74 row_shr:2 row_mask:0xf bank_mask:0xf
	s_nop 1
	v_add_u32_dpp v74, v74, v74 row_shr:4 row_mask:0xf bank_mask:0xf
	s_nop 1
	v_add_u32_dpp v74, v74, v74 row_shr:8 row_mask:0xf bank_mask:0xf
	s_nop 1
	v_add_u32_dpp v74, v74, v74 row_bcast:15 row_mask:0xa bank_mask:0xf
	s_nop 1
	v_add_u32_dpp v74, v74, v74 row_bcast:31 row_mask:0xc bank_mask:0xf
	v_mov_b32_e32 v108, -1
	v_mov_b32_e32 v109, 0
	v_readlane_b32 s13, v74, 63
	v_mov_b32_e32 v110, 0
	s_nop 0
	v_sub_u32_e32 v75, s13, v74
	v_add_u32_e32 v111, v75, v91
	v_cmp_gt_i32_e32 vcc, 0x100, v75
	v_cmp_le_i32_e64 s[0:1], s87, v111
	v_or_b32_e32 v112, 3, v6
	s_and_b64 vcc, vcc, s[0:1]
	v_cndmask_b32_e32 v108, v108, v112, vcc
	v_cndmask_b32_e32 v109, v109, v75, vcc
	v_cndmask_b32_e32 v110, v110, v91, vcc
	v_mov_b32_e32 v75, v111
	v_add_u32_e32 v111, v75, v90
	v_cmp_gt_i32_e32 vcc, 0x100, v75
	v_cmp_le_i32_e64 s[0:1], s87, v111
	v_or_b32_e32 v112, 2, v6
	s_and_b64 vcc, vcc, s[0:1]
	v_cndmask_b32_e32 v108, v108, v112, vcc
	v_cndmask_b32_e32 v109, v109, v75, vcc
	v_cndmask_b32_e32 v110, v110, v90, vcc
	v_mov_b32_e32 v75, v111
	v_add_u32_e32 v111, v75, v89
	v_cmp_gt_i32_e32 vcc, 0x100, v75
	v_cmp_le_i32_e64 s[0:1], s87, v111
	v_or_b32_e32 v112, 1, v6
	s_and_b64 vcc, vcc, s[0:1]
	v_cndmask_b32_e32 v108, v108, v112, vcc
	v_cndmask_b32_e32 v109, v109, v75, vcc
	v_cndmask_b32_e32 v110, v110, v89, vcc
	v_mov_b32_e32 v75, v111
	v_add_u32_e32 v111, v75, v88
	v_cmp_gt_i32_e32 vcc, 0x100, v75
	v_cmp_le_i32_e64 s[0:1], s87, v111
	v_or_b32_e32 v112, 0, v6
	s_and_b64 vcc, vcc, s[0:1]
	v_cndmask_b32_e32 v108, v108, v112, vcc
	v_cndmask_b32_e32 v109, v109, v75, vcc
	v_cndmask_b32_e32 v110, v110, v88, vcc
	v_mov_b32_e32 v75, v111
	v_cmp_lt_i32_e32 vcc, -1, v108
	s_ff1_i32_b64 s0, vcc
	s_cmp_lg_u64 vcc, 0
	s_cselect_b32 s0, s0, 0
	v_readlane_b32 s1, v109, s0
	v_readlane_b32 s12, v108, s0
	v_readlane_b32 s13, v110, s0
	s_sub_i32 s30, 0x100, s1
	s_nop 0
	v_mov_b32_e32 v114, s12
	v_mov_b32_e32 v115, s30
	v_mov_b32_e32 v116, s13
	s_and_saveexec_b64 s[0:1], s[26:27]
	ds_write_b128 v118, v[114:117] offset:48
	s_or_b64 exec, exec, s[0:1]
	v_add_u32_e32 v73, v92, v93
	v_add3_u32 v74, v73, v94, v95
	s_nop 1
	v_add_u32_dpp v74, v74, v74 row_shr:1 row_mask:0xf bank_mask:0xf
	s_nop 1
	v_add_u32_dpp v74, v74, v74 row_shr:2 row_mask:0xf bank_mask:0xf
	s_nop 1
	v_add_u32_dpp v74, v74, v74 row_shr:4 row_mask:0xf bank_mask:0xf
	s_nop 1
	v_add_u32_dpp v74, v74, v74 row_shr:8 row_mask:0xf bank_mask:0xf
	s_nop 1
	v_add_u32_dpp v74, v74, v74 row_bcast:15 row_mask:0xa bank_mask:0xf
	s_nop 1
	v_add_u32_dpp v74, v74, v74 row_bcast:31 row_mask:0xc bank_mask:0xf
	v_mov_b32_e32 v108, -1
	v_mov_b32_e32 v109, 0
	v_readlane_b32 s13, v74, 63
	v_mov_b32_e32 v110, 0
	s_nop 0
	v_sub_u32_e32 v75, s13, v74
	v_add_u32_e32 v111, v75, v95
	v_cmp_gt_i32_e32 vcc, 0x100, v75
	v_cmp_le_i32_e64 s[0:1], s87, v111
	v_or_b32_e32 v112, 3, v6
	s_and_b64 vcc, vcc, s[0:1]
	v_cndmask_b32_e32 v108, v108, v112, vcc
	v_cndmask_b32_e32 v109, v109, v75, vcc
	v_cndmask_b32_e32 v110, v110, v95, vcc
	v_mov_b32_e32 v75, v111
	v_add_u32_e32 v111, v75, v94
	v_cmp_gt_i32_e32 vcc, 0x100, v75
	v_cmp_le_i32_e64 s[0:1], s87, v111
	v_or_b32_e32 v112, 2, v6
	s_and_b64 vcc, vcc, s[0:1]
	v_cndmask_b32_e32 v108, v108, v112, vcc
	v_cndmask_b32_e32 v109, v109, v75, vcc
	v_cndmask_b32_e32 v110, v110, v94, vcc
	v_mov_b32_e32 v75, v111
	v_add_u32_e32 v111, v75, v93
	v_cmp_gt_i32_e32 vcc, 0x100, v75
	v_cmp_le_i32_e64 s[0:1], s87, v111
	v_or_b32_e32 v112, 1, v6
	s_and_b64 vcc, vcc, s[0:1]
	v_cndmask_b32_e32 v108, v108, v112, vcc
	v_cndmask_b32_e32 v109, v109, v75, vcc
	v_cndmask_b32_e32 v110, v110, v93, vcc
	v_mov_b32_e32 v75, v111
	v_add_u32_e32 v111, v75, v92
	v_cmp_gt_i32_e32 vcc, 0x100, v75
	v_cmp_le_i32_e64 s[0:1], s87, v111
	v_or_b32_e32 v112, 0, v6
	s_and_b64 vcc, vcc, s[0:1]
	v_cndmask_b32_e32 v108, v108, v112, vcc
	v_cndmask_b32_e32 v109, v109, v75, vcc
	v_cndmask_b32_e32 v110, v110, v92, vcc
	v_mov_b32_e32 v75, v111
	v_cmp_lt_i32_e32 vcc, -1, v108
	s_ff1_i32_b64 s0, vcc
	s_cmp_lg_u64 vcc, 0
	s_cselect_b32 s0, s0, 0
	v_readlane_b32 s1, v109, s0
	v_readlane_b32 s12, v108, s0
	v_readlane_b32 s13, v110, s0
	s_sub_i32 s30, 0x100, s1
	s_nop 0
	v_mov_b32_e32 v114, s12
	v_mov_b32_e32 v115, s30
	v_mov_b32_e32 v116, s13
	s_and_saveexec_b64 s[0:1], s[26:27]
	ds_write_b128 v118, v[114:117] offset:64
	s_or_b64 exec, exec, s[0:1]
	v_add_u32_e32 v73, v96, v97
	v_add3_u32 v74, v73, v98, v99
	s_nop 1
	v_add_u32_dpp v74, v74, v74 row_shr:1 row_mask:0xf bank_mask:0xf
	s_nop 1
	v_add_u32_dpp v74, v74, v74 row_shr:2 row_mask:0xf bank_mask:0xf
	s_nop 1
	v_add_u32_dpp v74, v74, v74 row_shr:4 row_mask:0xf bank_mask:0xf
	s_nop 1
	v_add_u32_dpp v74, v74, v74 row_shr:8 row_mask:0xf bank_mask:0xf
	s_nop 1
	v_add_u32_dpp v74, v74, v74 row_bcast:15 row_mask:0xa bank_mask:0xf
	s_nop 1
	v_add_u32_dpp v74, v74, v74 row_bcast:31 row_mask:0xc bank_mask:0xf
	v_mov_b32_e32 v108, -1
	v_mov_b32_e32 v109, 0
	v_readlane_b32 s13, v74, 63
	v_mov_b32_e32 v110, 0
	s_nop 0
	v_sub_u32_e32 v75, s13, v74
	v_add_u32_e32 v111, v75, v99
	v_cmp_gt_i32_e32 vcc, 0x100, v75
	v_cmp_le_i32_e64 s[0:1], s87, v111
	v_or_b32_e32 v112, 3, v6
	s_and_b64 vcc, vcc, s[0:1]
	v_cndmask_b32_e32 v108, v108, v112, vcc
	v_cndmask_b32_e32 v109, v109, v75, vcc
	v_cndmask_b32_e32 v110, v110, v99, vcc
	v_mov_b32_e32 v75, v111
	v_add_u32_e32 v111, v75, v98
	v_cmp_gt_i32_e32 vcc, 0x100, v75
	v_cmp_le_i32_e64 s[0:1], s87, v111
	v_or_b32_e32 v112, 2, v6
	s_and_b64 vcc, vcc, s[0:1]
	v_cndmask_b32_e32 v108, v108, v112, vcc
	v_cndmask_b32_e32 v109, v109, v75, vcc
	v_cndmask_b32_e32 v110, v110, v98, vcc
	v_mov_b32_e32 v75, v111
	v_add_u32_e32 v111, v75, v97
	v_cmp_gt_i32_e32 vcc, 0x100, v75
	v_cmp_le_i32_e64 s[0:1], s87, v111
	v_or_b32_e32 v112, 1, v6
	s_and_b64 vcc, vcc, s[0:1]
	v_cndmask_b32_e32 v108, v108, v112, vcc
	v_cndmask_b32_e32 v109, v109, v75, vcc
	v_cndmask_b32_e32 v110, v110, v97, vcc
	v_mov_b32_e32 v75, v111
	v_add_u32_e32 v111, v75, v96
	v_cmp_gt_i32_e32 vcc, 0x100, v75
	v_cmp_le_i32_e64 s[0:1], s87, v111
	v_or_b32_e32 v112, 0, v6
	s_and_b64 vcc, vcc, s[0:1]
	v_cndmask_b32_e32 v108, v108, v112, vcc
	v_cndmask_b32_e32 v109, v109, v75, vcc
	v_cndmask_b32_e32 v110, v110, v96, vcc
	v_mov_b32_e32 v75, v111
	v_cmp_lt_i32_e32 vcc, -1, v108
	s_ff1_i32_b64 s0, vcc
	s_cmp_lg_u64 vcc, 0
	s_cselect_b32 s0, s0, 0
	v_readlane_b32 s1, v109, s0
	v_readlane_b32 s12, v108, s0
	v_readlane_b32 s13, v110, s0
	s_sub_i32 s30, 0x100, s1
	s_nop 0
	v_mov_b32_e32 v114, s12
	v_mov_b32_e32 v115, s30
	v_mov_b32_e32 v116, s13
	s_and_saveexec_b64 s[0:1], s[26:27]
	ds_write_b128 v118, v[114:117] offset:80
	s_or_b64 exec, exec, s[0:1]
	v_add_u32_e32 v73, v100, v101
	v_add3_u32 v74, v73, v102, v103
	s_nop 1
	v_add_u32_dpp v74, v74, v74 row_shr:1 row_mask:0xf bank_mask:0xf
	s_nop 1
	v_add_u32_dpp v74, v74, v74 row_shr:2 row_mask:0xf bank_mask:0xf
	s_nop 1
	v_add_u32_dpp v74, v74, v74 row_shr:4 row_mask:0xf bank_mask:0xf
	s_nop 1
	v_add_u32_dpp v74, v74, v74 row_shr:8 row_mask:0xf bank_mask:0xf
	s_nop 1
	v_add_u32_dpp v74, v74, v74 row_bcast:15 row_mask:0xa bank_mask:0xf
	s_nop 1
	v_add_u32_dpp v74, v74, v74 row_bcast:31 row_mask:0xc bank_mask:0xf
	v_mov_b32_e32 v108, -1
	v_mov_b32_e32 v109, 0
	v_readlane_b32 s13, v74, 63
	v_mov_b32_e32 v110, 0
	s_nop 0
	v_sub_u32_e32 v75, s13, v74
	v_add_u32_e32 v111, v75, v103
	v_cmp_gt_i32_e32 vcc, 0x100, v75
	v_cmp_le_i32_e64 s[0:1], s87, v111
	v_or_b32_e32 v112, 3, v6
	s_and_b64 vcc, vcc, s[0:1]
	v_cndmask_b32_e32 v108, v108, v112, vcc
	v_cndmask_b32_e32 v109, v109, v75, vcc
	v_cndmask_b32_e32 v110, v110, v103, vcc
	v_mov_b32_e32 v75, v111
	v_add_u32_e32 v111, v75, v102
	v_cmp_gt_i32_e32 vcc, 0x100, v75
	v_cmp_le_i32_e64 s[0:1], s87, v111
	v_or_b32_e32 v112, 2, v6
	s_and_b64 vcc, vcc, s[0:1]
	v_cndmask_b32_e32 v108, v108, v112, vcc
	v_cndmask_b32_e32 v109, v109, v75, vcc
	v_cndmask_b32_e32 v110, v110, v102, vcc
	v_mov_b32_e32 v75, v111
	v_add_u32_e32 v111, v75, v101
	v_cmp_gt_i32_e32 vcc, 0x100, v75
	v_cmp_le_i32_e64 s[0:1], s87, v111
	v_or_b32_e32 v112, 1, v6
	s_and_b64 vcc, vcc, s[0:1]
	v_cndmask_b32_e32 v108, v108, v112, vcc
	v_cndmask_b32_e32 v109, v109, v75, vcc
	v_cndmask_b32_e32 v110, v110, v101, vcc
	v_mov_b32_e32 v75, v111
	v_add_u32_e32 v111, v75, v100
	v_cmp_gt_i32_e32 vcc, 0x100, v75
	v_cmp_le_i32_e64 s[0:1], s87, v111
	v_or_b32_e32 v112, 0, v6
	s_and_b64 vcc, vcc, s[0:1]
	v_cndmask_b32_e32 v108, v108, v112, vcc
	v_cndmask_b32_e32 v109, v109, v75, vcc
	v_cndmask_b32_e32 v110, v110, v100, vcc
	v_mov_b32_e32 v75, v111
	v_cmp_lt_i32_e32 vcc, -1, v108
	s_ff1_i32_b64 s0, vcc
	s_cmp_lg_u64 vcc, 0
	s_cselect_b32 s0, s0, 0
	v_readlane_b32 s1, v109, s0
	v_readlane_b32 s12, v108, s0
	v_readlane_b32 s13, v110, s0
	s_sub_i32 s30, 0x100, s1
	s_nop 0
	v_mov_b32_e32 v114, s12
	v_mov_b32_e32 v115, s30
	v_mov_b32_e32 v116, s13
	s_and_saveexec_b64 s[0:1], s[26:27]
	ds_write_b128 v118, v[114:117] offset:96
	s_or_b64 exec, exec, s[0:1]
	v_add_u32_e32 v73, v104, v105
	v_add3_u32 v74, v73, v106, v107
	s_nop 1
	v_add_u32_dpp v74, v74, v74 row_shr:1 row_mask:0xf bank_mask:0xf
	s_nop 1
	v_add_u32_dpp v74, v74, v74 row_shr:2 row_mask:0xf bank_mask:0xf
	s_nop 1
	v_add_u32_dpp v74, v74, v74 row_shr:4 row_mask:0xf bank_mask:0xf
	s_nop 1
	v_add_u32_dpp v74, v74, v74 row_shr:8 row_mask:0xf bank_mask:0xf
	s_nop 1
	v_add_u32_dpp v74, v74, v74 row_bcast:15 row_mask:0xa bank_mask:0xf
	s_nop 1
	v_add_u32_dpp v74, v74, v74 row_bcast:31 row_mask:0xc bank_mask:0xf
	v_mov_b32_e32 v108, -1
	v_mov_b32_e32 v109, 0
	v_readlane_b32 s13, v74, 63
	v_mov_b32_e32 v110, 0
	s_nop 0
	v_sub_u32_e32 v75, s13, v74
	v_add_u32_e32 v111, v75, v107
	v_cmp_gt_i32_e32 vcc, 0x100, v75
	v_cmp_le_i32_e64 s[0:1], s87, v111
	v_or_b32_e32 v112, 3, v6
	s_and_b64 vcc, vcc, s[0:1]
	v_cndmask_b32_e32 v108, v108, v112, vcc
	v_cndmask_b32_e32 v109, v109, v75, vcc
	v_cndmask_b32_e32 v110, v110, v107, vcc
	v_mov_b32_e32 v75, v111
	v_add_u32_e32 v111, v75, v106
	v_cmp_gt_i32_e32 vcc, 0x100, v75
	v_cmp_le_i32_e64 s[0:1], s87, v111
	v_or_b32_e32 v112, 2, v6
	s_and_b64 vcc, vcc, s[0:1]
	v_cndmask_b32_e32 v108, v108, v112, vcc
	v_cndmask_b32_e32 v109, v109, v75, vcc
	v_cndmask_b32_e32 v110, v110, v106, vcc
	v_mov_b32_e32 v75, v111
	v_add_u32_e32 v111, v75, v105
	v_cmp_gt_i32_e32 vcc, 0x100, v75
	v_cmp_le_i32_e64 s[0:1], s87, v111
	v_or_b32_e32 v112, 1, v6
	s_and_b64 vcc, vcc, s[0:1]
	v_cndmask_b32_e32 v108, v108, v112, vcc
	v_cndmask_b32_e32 v109, v109, v75, vcc
	v_cndmask_b32_e32 v110, v110, v105, vcc
	v_mov_b32_e32 v75, v111
	v_add_u32_e32 v111, v75, v104
	v_cmp_gt_i32_e32 vcc, 0x100, v75
	v_cmp_le_i32_e64 s[0:1], s87, v111
	v_or_b32_e32 v112, 0, v6
	s_and_b64 vcc, vcc, s[0:1]
	v_cndmask_b32_e32 v108, v108, v112, vcc
	v_cndmask_b32_e32 v109, v109, v75, vcc
	v_cndmask_b32_e32 v110, v110, v104, vcc
	v_mov_b32_e32 v75, v111
	v_cmp_lt_i32_e32 vcc, -1, v108
	s_ff1_i32_b64 s0, vcc
	s_cmp_lg_u64 vcc, 0
	s_cselect_b32 s0, s0, 0
	v_readlane_b32 s1, v109, s0
	v_readlane_b32 s12, v108, s0
	v_readlane_b32 s13, v110, s0
	s_sub_i32 s30, 0x100, s1
	s_nop 0
	v_mov_b32_e32 v114, s12
	v_mov_b32_e32 v115, s30
	v_mov_b32_e32 v116, s13
	s_and_saveexec_b64 s[0:1], s[26:27]
	ds_write_b128 v118, v[114:117] offset:112
	s_or_b64 exec, exec, s[0:1]
	s_branch .Lthr_done_a
.Lthr_none_a:
	s_lshl_b32 s31, s96, 7
	s_add_i32 s31, s31, 0x23000
	v_mov_b32_e32 v118, s31
	v_mov_b32_e32 v114, -1
	v_mov_b32_e32 v115, 0
	v_mov_b32_e32 v116, 0
	v_mov_b32_e32 v117, 0
	s_and_saveexec_b64 s[0:1], s[26:27]
	ds_write_b128 v118, v[114:117]
	ds_write_b128 v118, v[114:117] offset:16
	ds_write_b128 v118, v[114:117] offset:32
	ds_write_b128 v118, v[114:117] offset:48
	ds_write_b128 v118, v[114:117] offset:64
	ds_write_b128 v118, v[114:117] offset:80
	ds_write_b128 v118, v[114:117] offset:96
	ds_write_b128 v118, v[114:117] offset:112
	s_or_b64 exec, exec, s[0:1]
.Lthr_done_a:
	s_mov_b64 s[0:1], 0
.LBB0_542:
	s_or_b64 exec, exec, s[0:1]
	s_waitcnt lgkmcnt(0)
	s_barrier
	s_and_saveexec_b64 s[0:1], s[28:29]
	s_movk_i32 s16, 0x1dff
	s_cbranch_execz .LBB0_545
	v_readlane_b32 s12, v253, 43
	s_nop 1
	v_add_u32_e32 v2, s12, v6
	v_readlane_b32 s12, v253, 44
	s_nop 1
	v_add_u32_e32 v3, s12, v42
	s_mov_b64 s[12:13], 0

.Lthr_done_b:
	s_mov_b64 s[0:1], 0
.LBB0_920:
	s_or_b64 exec, exec, s[0:1]
	s_waitcnt lgkmcnt(0)
	s_barrier
	s_and_saveexec_b64 s[0:1], s[28:29]
	s_movk_i32 s16, 0x1dff
	s_cbranch_execz .LBB0_923
	v_readlane_b32 s12, v253, 43
	s_nop 1
	v_add_u32_e32 v2, s12, v6
	v_readlane_b32 s12, v253, 44
	s_nop 1
	v_add_u32_e32 v3, s12, v42
	s_mov_b64 s[12:13], 0
